# baseline (speedup 1.0000x reference)
.LBB0_10:
	s_or_b64 exec, exec, s[8:9]
	s_waitcnt vmcnt(0)
	v_cvt_pk_f16_f32 v9, v8, v9
	v_cvt_pk_f16_f32 v8, v6, v7
	v_cvt_pk_f16_f32 v6, v2, v3
	v_lshrrev_b32_e32 v2, 6, v1
	v_ashrrev_i32_e32 v3, 5, v13
	v_cvt_pk_f16_f32 v7, v4, v5
	v_mad_i32_i24 v4, v2, 10, v3
	s_movk_i32 s3, 0x3000
	v_mov_b64_e32 v[2:3], s[6:7]
	v_mad_i64_i32 v[2:3], s[6:7], v4, s3, v[2:3]
	v_lshlrev_b32_e32 v4, 12, v12
	v_ashrrev_i32_e32 v5, 31, v4
	v_lshl_add_u64 v[2:3], v[2:3], 0, v[4:5]
	v_lshlrev_b32_e32 v4, 6, v1
	v_lshlrev_b32_e32 v10, 4, v0
	v_lshlrev_b32_e32 v1, 3, v1
	v_and_b32_e32 v5, 0x3c0, v4
	v_and_b32_e32 v10, 48, v10
	v_and_b32_e32 v1, 32, v1
	v_bitop3_b32 v1, v5, v1, v10 bitop3:0x36
	s_movk_i32 s3, 0xc00
	v_and_or_b32 v4, v4, s3, v1
	v_mov_b32_e32 v5, 0
	v_lshl_add_u64 v[2:3], v[2:3], 0, v[4:5]
	global_store_dwordx4 v[2:3], v[6:9], off sc1

.LBB0_19:
	s_or_b64 exec, exec, s[2:3]
	v_mul_u32_u24_e32 v14, 0x52800, v11
	s_waitcnt vmcnt(0)
	v_cvt_pk_f16_f32 v9, v8, v9
	v_cvt_pk_f16_f32 v8, v6, v7
	v_cvt_pk_f16_f32 v6, v2, v3
	s_waitcnt lgkmcnt(0)
	v_lshl_add_u64 v[2:3], s[0:1], 0, v[14:15]
	v_ashrrev_i32_e32 v1, 2, v1
	v_ashrrev_i32_e32 v11, 31, v10
	s_movk_i32 s0, 0x210
	v_cvt_pk_f16_f32 v7, v4, v5
	v_mad_i64_i32 v[4:5], s[0:1], v1, s0, v[10:11]
	v_lshlrev_b64 v[4:5], 6, v[4:5]
	v_lshlrev_b32_e32 v0, 4, v0
	v_lshl_add_u64 v[2:3], v[2:3], 0, v[4:5]
	v_and_b32_e32 v14, 48, v0
	v_lshl_add_u64 v[0:1], v[2:3], 0, v[14:15]
	global_store_dwordx4 v[0:1], v[6:9], off sc1
	s_endpgm
	.p2align	8
